# speedup vs baseline: 1.0054x; 1.0041x over previous
.LBB2_13:
	v_exp_f32_e32 v48, v48
	v_exp_f32_e32 v49, v49
	v_mfma_f32_32x32x16_bf16 v[112:127], a[192:195], a[128:131], v[16:31]
	ds_read_b64_tr_b16 v[180:181], v223 offset:0
	v_cvt_pk_bf16_f32 v164, v128, v129
	v_exp_f32_e32 v50, v50
	v_exp_f32_e32 v51, v51
	v_mfma_f32_32x32x16_bf16 v[96:111], a[192:195], a[160:163], v[0:15]
	ds_read_b64_tr_b16 v[182:183], v223 offset:0x800
	v_cvt_pk_bf16_f32 v165, v130, v131
	v_mfma_f32_32x32x16_bf16 v[80:95], a[224:227], a[128:131], v[16:31]
	ds_read_b64_tr_b16 v[184:185], v223 offset:0x200
	v_exp_f32_e32 v236, v52
	v_exp_f32_e32 v237, v53
	v_cvt_pk_bf16_f32 v166, v132, v133
	v_mfma_f32_32x32x16_bf16 v[64:79], a[224:227], a[160:163], v[0:15]
	ds_read_b64_tr_b16 v[186:187], v223 offset:0xa00
	ds_read_b64_tr_b16 v[176:177], v223 offset:0x400
	v_exp_f32_e32 v242, v54
	v_exp_f32_e32 v243, v55
	v_cvt_pk_bf16_f32 v167, v134, v135
	v_exp_f32_e32 v198, v56
	v_exp_f32_e32 v199, v57
	v_mfma_f32_32x32x16_bf16 v[112:127], a[196:199], a[132:135], v[112:127]
	ds_read_b64_tr_b16 v[178:179], v223 offset:0xc00
	v_cvt_pk_bf16_f32 v128, v136, v137
	v_exp_f32_e32 v230, v58
	v_exp_f32_e32 v231, v59
	v_mfma_f32_32x32x16_bf16 v[96:111], a[196:199], a[164:167], v[96:111]
	ds_read_b64_tr_b16 v[188:189], v223 offset:0x600
	v_cvt_pk_bf16_f32 v129, v138, v139
	v_exp_f32_e32 v232, v60
	v_exp_f32_e32 v233, v61
	v_mfma_f32_32x32x16_bf16 v[80:95], a[228:231], a[132:135], v[80:95]
	ds_read_b64_tr_b16 v[190:191], v223 offset:0xe00
	v_cvt_pk_bf16_f32 v130, v140, v141
	v_mfma_f32_32x32x16_bf16 v[64:79], a[228:231], a[164:167], v[64:79]
	ds_read_b64_tr_b16 v[172:173], v223 offset:0x1000
	v_exp_f32_e32 v234, v62
	v_exp_f32_e32 v235, v63
	ds_read_b64_tr_b16 v[174:175], v223 offset:0x1800
	v_cvt_pk_bf16_f32 v131, v142, v143
	v_exp_f32_e32 v141, v32
	v_exp_f32_e32 v142, v33
	v_mfma_f32_32x32x16_bf16 v[112:127], a[200:203], a[136:139], v[112:127]
	ds_read_b64_tr_b16 v[168:169], v223 offset:0x1200
	v_cvt_pk_bf16_f32 v192, v144, v145
	v_exp_f32_e32 v143, v34
	v_mfma_f32_32x32x16_bf16 v[96:111], a[200:203], a[168:171], v[96:111]
	ds_read_b64_tr_b16 v[170:171], v223 offset:0x1a00
	v_exp_f32_e32 v244, v35
	v_cvt_pk_bf16_f32 v193, v146, v147
	v_mfma_f32_32x32x16_bf16 v[80:95], a[232:235], a[136:139], v[80:95]
	ds_read_b64_tr_b16 v[160:161], v223 offset:0x1400
	v_exp_f32_e32 v245, v36
	v_exp_f32_e32 v246, v37
	v_cvt_pk_bf16_f32 v194, v148, v149
	v_mfma_f32_32x32x16_bf16 v[64:79], a[232:235], a[168:171], v[64:79]
	ds_read_b64_tr_b16 v[162:163], v223 offset:0x1c00
	ds_read_b64_tr_b16 v[136:137], v223 offset:0x1600
	v_exp_f32_e32 v247, v38
	v_exp_f32_e32 v248, v39
	v_cvt_pk_bf16_f32 v195, v150, v151
	v_exp_f32_e32 v148, v40
	v_exp_f32_e32 v149, v41
	v_mfma_f32_32x32x16_bf16 v[112:127], a[204:207], a[140:143], v[112:127]
	ds_read_b64_tr_b16 v[138:139], v223 offset:0x1e00
	v_cvt_pk_bf16_f32 v144, v152, v153
	v_exp_f32_e32 v150, v42
	v_exp_f32_e32 v151, v43
	v_mfma_f32_32x32x16_bf16 v[96:111], a[204:207], a[172:175], v[96:111]
	ds_read_b64_tr_b16 v[132:133], v223 offset:0x2000
	v_cvt_pk_bf16_f32 v145, v154, v155
	v_exp_f32_e32 v152, v44
	v_exp_f32_e32 v153, v45
	v_mfma_f32_32x32x16_bf16 v[80:95], a[236:239], a[140:143], v[80:95]
	ds_read_b64_tr_b16 v[134:135], v223 offset:0x2800
	v_cvt_pk_bf16_f32 v146, v156, v157
	v_mfma_f32_32x32x16_bf16 v[64:79], a[236:239], a[172:175], v[64:79]
	ds_read_b64_tr_b16 v[60:61], v223 offset:0x2200
	v_exp_f32_e32 v154, v46
	v_exp_f32_e32 v155, v47
	ds_read_b64_tr_b16 v[62:63], v223 offset:0x2a00
	v_cvt_pk_bf16_f32 v147, v158, v159
	s_mov_b32 s0, s30
	v_mfma_f32_32x32x16_bf16 v[112:127], a[208:211], a[144:147], v[112:127]
	ds_read_b64_tr_b16 v[56:57], v223 offset:0x2400
	v_cvt_pk_bf16_f32 v52, v48, v49
	v_add_f32_e32 v32, v239, v48
	v_add_f32_e32 v33, v238, v49
	s_add_i32 s19, s17, 0xfffda000
	s_mov_b32 s1, s19
	v_mfma_f32_32x32x16_bf16 v[96:111], a[208:211], a[176:179], v[96:111]
	ds_read_b64_tr_b16 v[58:59], v223 offset:0x2c00
	v_cvt_pk_bf16_f32 v53, v50, v51
	v_add_f32_e32 v32, v32, v50
	v_add_f32_e32 v33, v33, v51
	s_mov_b32 s81, s37
	v_mfma_f32_32x32x16_bf16 v[80:95], a[240:243], a[144:147], v[80:95]
	ds_read_b64_tr_b16 v[48:49], v223 offset:0x2600
	v_cvt_pk_bf16_f32 v54, v236, v237
	v_add_f32_e32 v32, v32, v236
	v_add_f32_e32 v33, v33, v237
	s_add_i32 s82, s17, 0xfffdc000
	v_mfma_f32_32x32x16_bf16 v[64:79], a[240:243], a[176:179], v[64:79]
	ds_read_b64_tr_b16 v[50:51], v223 offset:0x2e00
	ds_read_b64_tr_b16 v[44:45], v223 offset:0x3000
	v_cvt_pk_bf16_f32 v55, v242, v243
	v_add_f32_e32 v32, v32, v242
	v_add_f32_e32 v33, v33, v243
	s_mov_b32 s83, s39
	v_mfma_f32_32x32x16_bf16 v[112:127], a[212:215], a[148:151], v[112:127]
	ds_read_b64_tr_b16 v[46:47], v223 offset:0x3800
	v_add_f32_e32 v32, v32, v198
	v_add_f32_e32 v33, v33, v199
	s_add_i32 s24, s17, 0xfffde000
	s_mov_b32 s84, s24
	v_mfma_f32_32x32x16_bf16 v[96:111], a[212:215], a[180:183], v[96:111]
	ds_read_b64_tr_b16 v[40:41], v223 offset:0x3200
	v_add_f32_e32 v32, v32, v230
	v_add_f32_e32 v33, v33, v231
	s_mov_b32 s85, s41
	v_mfma_f32_32x32x16_bf16 v[80:95], a[244:247], a[148:151], v[80:95]
	ds_read_b64_tr_b16 v[42:43], v223 offset:0x3a00
	v_add_f32_e32 v32, v32, v232
	v_add_f32_e32 v33, v33, v233
	s_add_i32 s86, s17, 0xfffe0000
	v_mfma_f32_32x32x16_bf16 v[64:79], a[244:247], a[180:183], v[64:79]
	ds_read_b64_tr_b16 v[36:37], v223 offset:0x3400
	ds_read_b64_tr_b16 v[38:39], v223 offset:0x3c00
	v_add_f32_e32 v156, v32, v234
	v_add_f32_e32 v157, v33, v235
	s_mov_b32 s87, s43
	v_mfma_f32_32x32x16_bf16 v[112:127], a[216:219], a[152:155], v[112:127]
	ds_read_b64_tr_b16 v[32:33], v223 offset:0x3600
	v_cvt_pk_bf16_f32 v140, v141, v142
	v_add_f32_e32 v158, v240, v141
	v_add_f32_e32 v142, v241, v142
	s_add_i32 s88, s17, 0xfffba000
	v_mfma_f32_32x32x16_bf16 v[96:111], a[216:219], a[184:187], v[96:111]
	ds_read_b64_tr_b16 v[34:35], v223 offset:0x3e00
	v_cvt_pk_bf16_f32 v141, v143, v244
	v_add_f32_e32 v143, v158, v143
	v_add_f32_e32 v158, v142, v244
	v_mfma_f32_32x32x16_bf16 v[80:95], a[248:251], a[152:155], v[80:95]
	s_mov_b32 s89, s45
	v_cvt_pk_bf16_f32 v142, v245, v246
	v_add_f32_e32 v159, v143, v245
	v_add_f32_e32 v158, v158, v246
	v_mfma_f32_32x32x16_bf16 v[64:79], a[248:251], a[184:187], v[64:79]
	s_add_i32 s90, s17, 0xfffba080
	v_cvt_pk_bf16_f32 v143, v247, v248
	v_add_f32_e32 v159, v159, v247
	v_add_f32_e32 v158, v158, v248
	v_mfma_f32_32x32x16_bf16 v[112:127], a[220:223], a[156:159], v[112:127]
	s_mov_b32 s91, s47
	v_add_f32_e32 v159, v159, v148
	v_add_f32_e32 v158, v158, v149
	v_mfma_f32_32x32x16_bf16 v[96:111], a[220:223], a[188:191], v[96:111]
	s_add_i32 s92, s17, 0xfffbe000
	v_add_f32_e32 v159, v159, v150
	v_add_f32_e32 v158, v158, v151
	v_mfma_f32_32x32x16_bf16 v[80:95], a[252:255], a[156:159], v[80:95]
	s_mov_b32 s93, s49
	v_add_f32_e32 v159, v159, v152
	v_add_f32_e32 v158, v158, v153
	v_mfma_f32_32x32x16_bf16 v[64:79], a[252:255], a[188:191], v[64:79]
	s_add_i32 s94, s17, 0xfffbe080
	v_add_f32_e32 v159, v159, v154
	v_add_f32_e32 v158, v158, v155
	v_add_f32_e32 v156, v156, v157
	s_waitcnt vmcnt(0) lgkmcnt(0)
	s_barrier
	v_add_f32_e32 v158, v159, v158
	v_mov_b32_e32 v157, v156
	v_mov_b32_e32 v159, v158
	s_nop 0
	v_permlane32_swap_b32_e32 v156, v157
	v_permlane32_swap_b32_e32 v158, v159
	v_add_f32_e32 v156, v156, v157
	v_add_f32_e32 v158, v158, v159
	v_add_f32_e32 v197, v197, v156
	v_add_f32_e32 v196, v196, v158
	s_mov_b32 m0, s0
	v_mfma_f32_32x32x16_bf16 a[0:15], v[180:183], v[164:167], a[0:15]
	buffer_load_dwordx4 v209, s[4:7], s1 offen lds
	s_mov_b32 m0, s81
	v_mfma_f32_32x32x16_bf16 a[16:31], v[180:183], v[192:195], a[16:31]
	buffer_load_dwordx4 v210, s[4:7], s82 offen lds
	ds_read_b128 a[192:195], v219 offset:0
	s_mov_b32 m0, s83
	v_mfma_f32_32x32x16_bf16 a[32:47], v[184:187], v[164:167], a[32:47]
	buffer_load_dwordx4 v209, s[4:7], s84 offen lds
	ds_read_b128 a[196:199], v220 offset:0
	s_mov_b32 m0, s85
	v_mfma_f32_32x32x16_bf16 a[48:63], v[184:187], v[192:195], a[48:63]
	buffer_load_dwordx4 v210, s[4:7], s86 offen lds
	ds_read_b128 a[200:203], v221 offset:0
	s_mov_b32 m0, s87
	v_mfma_f32_32x32x16_bf16 a[64:79], v[176:179], v[164:167], a[64:79]
	buffer_load_dwordx4 v211, s[20:23], s88 offen lds
	ds_read_b128 a[204:207], v222 offset:0
	s_mov_b32 m0, s89
	v_mfma_f32_32x32x16_bf16 a[80:95], v[176:179], v[192:195], a[80:95]
	buffer_load_dwordx4 v211, s[20:23], s90 offen lds
	ds_read_b128 a[208:211], v219 offset:128
	s_mov_b32 m0, s91
	v_mfma_f32_32x32x16_bf16 a[96:111], v[188:191], v[164:167], a[96:111]
	buffer_load_dwordx4 v211, s[20:23], s92 offen lds
	ds_read_b128 a[212:215], v220 offset:128
	s_mov_b32 m0, s93
	v_mfma_f32_32x32x16_bf16 a[112:127], v[188:191], v[192:195], a[112:127]
	buffer_load_dwordx4 v211, s[20:23], s94 offen lds
	ds_read_b128 a[216:219], v221 offset:128
	v_mfma_f32_32x32x16_bf16 a[0:15], v[172:175], v[128:131], a[0:15]
	ds_read_b128 a[220:223], v222 offset:128
	v_max3_f32 v156, v112, v113, v80
	v_max3_f32 v157, v114, v115, v81
	v_max3_f32 v156, v156, v82, v83
	v_mfma_f32_32x32x16_bf16 a[16:31], v[172:175], v[144:147], a[16:31]
	ds_read_b128 a[224:227], v219 offset:8192
	v_max3_f32 v156, v156, v116, v117
	v_max3_f32 v157, v157, v118, v119
	v_max3_f32 v156, v156, v84, v85
	v_max3_f32 v157, v157, v86, v87
	v_mfma_f32_32x32x16_bf16 a[32:47], v[168:171], v[128:131], a[32:47]
	ds_read_b128 a[228:231], v220 offset:8192
	v_max3_f32 v156, v156, v120, v121
	v_max3_f32 v157, v157, v122, v123
	v_max3_f32 v156, v156, v88, v89
	v_max3_f32 v157, v157, v90, v91
	v_mfma_f32_32x32x16_bf16 a[48:63], v[168:171], v[144:147], a[48:63]
	ds_read_b128 a[232:235], v221 offset:8192
	v_max3_f32 v156, v156, v124, v125
	v_max3_f32 v157, v157, v126, v127
	v_max3_f32 v156, v156, v92, v93
	v_max3_f32 v157, v157, v94, v95
	v_mfma_f32_32x32x16_bf16 a[64:79], v[160:163], v[128:131], a[64:79]
	ds_read_b128 a[236:239], v222 offset:8192
	v_max3_f32 v158, v96, v97, v64
	v_max3_f32 v159, v98, v99, v65
	v_max3_f32 v158, v158, v66, v67
	v_mfma_f32_32x32x16_bf16 a[80:95], v[160:163], v[144:147], a[80:95]
	ds_read_b128 a[240:243], v219 offset:8320
	v_max3_f32 v158, v158, v100, v101
	v_max3_f32 v159, v159, v102, v103
	v_max3_f32 v158, v158, v68, v69
	v_max3_f32 v159, v159, v70, v71
	v_mfma_f32_32x32x16_bf16 a[96:111], v[136:139], v[128:131], a[96:111]
	ds_read_b128 a[244:247], v220 offset:8320
	v_max3_f32 v128, v158, v104, v105
	v_max3_f32 v129, v159, v106, v107
	v_max3_f32 v128, v128, v72, v73
	v_max3_f32 v129, v129, v74, v75
	v_mfma_f32_32x32x16_bf16 a[112:127], v[136:139], v[144:147], a[112:127]
	ds_read_b128 a[248:251], v221 offset:8320
	v_max3_f32 v128, v128, v108, v109
	v_max3_f32 v129, v129, v110, v111
	v_max3_f32 v128, v128, v76, v77
	v_max3_f32 v130, v129, v78, v79
	v_mfma_f32_32x32x16_bf16 a[0:15], v[132:135], v[52:55], a[0:15]
	ds_read_b128 a[252:255], v222 offset:8320
	v_max_f32_e32 v129, v156, v157
	v_mov_b32_e32 v131, v129
	s_nop 1
	v_permlane32_swap_b32_e32 v129, v131
	v_max_f32_e32 v129, v129, v131
	v_mfma_f32_32x32x16_bf16 a[16:31], v[132:135], v[140:143], a[16:31]
	v_max_f32_e32 v128, v128, v130
	v_mov_b32_e32 v130, v128
	s_nop 1
	v_permlane32_swap_b32_e32 v128, v130
	v_max_f32_e32 v128, v128, v130
	v_max_f32_e32 v130, v129, v129
	v_max_f32_e32 v131, v128, v128
	v_max_f32_e32 v130, v130, v131
	v_mfma_f32_32x32x16_bf16 a[32:47], v[60:63], v[52:55], a[32:47]
	v_cmp_lt_f32_e32 vcc, s79, v130
	s_cmp_lg_u64 vcc, 0
	s_cselect_b64 s[0:1], -1, 0
	s_cbranch_vccnz .LBB2_18

.LBB2_15:
	s_waitcnt lgkmcnt(0)
	v_exp_f32_e32 v80, v80
	v_exp_f32_e32 v81, v81
	v_mfma_f32_32x32x16_bf16 v[112:127], a[192:195], a[128:131], v[16:31]
	ds_read_b64_tr_b16 v[180:181], v208 offset:0
	v_cvt_pk_bf16_f32 v164, v128, v129
	v_exp_f32_e32 v82, v82
	v_exp_f32_e32 v83, v83
	v_mfma_f32_32x32x16_bf16 v[96:111], a[192:195], a[160:163], v[0:15]
	ds_read_b64_tr_b16 v[182:183], v208 offset:0x800
	v_cvt_pk_bf16_f32 v165, v130, v131
	v_mfma_f32_32x32x16_bf16 v[48:63], a[224:227], a[128:131], v[16:31]
	ds_read_b64_tr_b16 v[184:185], v208 offset:0x200
	v_exp_f32_e32 v240, v84
	v_exp_f32_e32 v241, v85
	v_cvt_pk_bf16_f32 v166, v132, v133
	v_mfma_f32_32x32x16_bf16 v[32:47], a[224:227], a[160:163], v[0:15]
	ds_read_b64_tr_b16 v[186:187], v208 offset:0xa00
	ds_read_b64_tr_b16 v[176:177], v208 offset:0x400
	v_exp_f32_e32 v242, v86
	v_exp_f32_e32 v243, v87
	v_cvt_pk_bf16_f32 v167, v134, v135
	v_exp_f32_e32 v198, v88
	v_exp_f32_e32 v199, v89
	v_mfma_f32_32x32x16_bf16 v[112:127], a[196:199], a[132:135], v[112:127]
	ds_read_b64_tr_b16 v[178:179], v208 offset:0xc00
	v_cvt_pk_bf16_f32 v128, v136, v137
	v_exp_f32_e32 v230, v90
	v_exp_f32_e32 v231, v91
	v_mfma_f32_32x32x16_bf16 v[96:111], a[196:199], a[164:167], v[96:111]
	ds_read_b64_tr_b16 v[188:189], v208 offset:0x600
	v_cvt_pk_bf16_f32 v129, v138, v139
	v_exp_f32_e32 v232, v92
	v_exp_f32_e32 v233, v93
	v_mfma_f32_32x32x16_bf16 v[48:63], a[228:231], a[132:135], v[48:63]
	ds_read_b64_tr_b16 v[190:191], v208 offset:0xe00
	v_cvt_pk_bf16_f32 v130, v140, v141
	v_mfma_f32_32x32x16_bf16 v[32:47], a[228:231], a[164:167], v[32:47]
	ds_read_b64_tr_b16 v[172:173], v208 offset:0x1000
	v_exp_f32_e32 v234, v94
	v_exp_f32_e32 v235, v95
	ds_read_b64_tr_b16 v[174:175], v208 offset:0x1800
	v_cvt_pk_bf16_f32 v131, v142, v143
	v_exp_f32_e32 v141, v64
	v_exp_f32_e32 v142, v65
	v_mfma_f32_32x32x16_bf16 v[112:127], a[200:203], a[136:139], v[112:127]
	ds_read_b64_tr_b16 v[168:169], v208 offset:0x1200
	v_cvt_pk_bf16_f32 v192, v144, v145
	v_exp_f32_e32 v143, v66
	v_mfma_f32_32x32x16_bf16 v[96:111], a[200:203], a[168:171], v[96:111]
	ds_read_b64_tr_b16 v[170:171], v208 offset:0x1a00
	v_exp_f32_e32 v244, v67
	v_cvt_pk_bf16_f32 v193, v146, v147
	v_mfma_f32_32x32x16_bf16 v[48:63], a[232:235], a[136:139], v[48:63]
	ds_read_b64_tr_b16 v[160:161], v208 offset:0x1400
	v_exp_f32_e32 v245, v68
	v_exp_f32_e32 v246, v69
	v_cvt_pk_bf16_f32 v194, v148, v149
	v_mfma_f32_32x32x16_bf16 v[32:47], a[232:235], a[168:171], v[32:47]
	ds_read_b64_tr_b16 v[162:163], v208 offset:0x1c00
	ds_read_b64_tr_b16 v[136:137], v208 offset:0x1600
	v_exp_f32_e32 v247, v70
	v_exp_f32_e32 v248, v71
	v_cvt_pk_bf16_f32 v195, v150, v151
	v_exp_f32_e32 v148, v72
	v_exp_f32_e32 v149, v73
	v_mfma_f32_32x32x16_bf16 v[112:127], a[204:207], a[140:143], v[112:127]
	ds_read_b64_tr_b16 v[138:139], v208 offset:0x1e00
	v_cvt_pk_bf16_f32 v144, v152, v153
	v_exp_f32_e32 v150, v74
	v_exp_f32_e32 v151, v75
	v_mfma_f32_32x32x16_bf16 v[96:111], a[204:207], a[172:175], v[96:111]
	ds_read_b64_tr_b16 v[132:133], v208 offset:0x2000
	v_cvt_pk_bf16_f32 v145, v154, v155
	v_exp_f32_e32 v152, v76
	v_exp_f32_e32 v153, v77
	v_mfma_f32_32x32x16_bf16 v[48:63], a[236:239], a[140:143], v[48:63]
	ds_read_b64_tr_b16 v[134:135], v208 offset:0x2800
	v_cvt_pk_bf16_f32 v146, v156, v157
	v_mfma_f32_32x32x16_bf16 v[32:47], a[236:239], a[172:175], v[32:47]
	ds_read_b64_tr_b16 v[92:93], v208 offset:0x2200
	v_exp_f32_e32 v154, v78
	v_exp_f32_e32 v155, v79
	ds_read_b64_tr_b16 v[94:95], v208 offset:0x2a00
	v_cvt_pk_bf16_f32 v147, v158, v159
	s_mov_b32 s0, s51
	v_mfma_f32_32x32x16_bf16 v[112:127], a[208:211], a[144:147], v[112:127]
	ds_read_b64_tr_b16 v[88:89], v208 offset:0x2400
	v_cvt_pk_bf16_f32 v84, v80, v81
	v_add_f32_e32 v64, v237, v80
	v_add_f32_e32 v65, v236, v81
	s_add_i32 s1, s17, 0xffffa000
	v_mfma_f32_32x32x16_bf16 v[96:111], a[208:211], a[176:179], v[96:111]
	ds_read_b64_tr_b16 v[90:91], v208 offset:0x2c00
	v_cvt_pk_bf16_f32 v85, v82, v83
	v_add_f32_e32 v64, v64, v82
	v_add_f32_e32 v65, v65, v83
	s_mov_b32 s81, s53
	v_mfma_f32_32x32x16_bf16 v[48:63], a[240:243], a[144:147], v[48:63]
	ds_read_b64_tr_b16 v[80:81], v208 offset:0x2600
	v_cvt_pk_bf16_f32 v86, v240, v241
	v_add_f32_e32 v64, v64, v240
	v_add_f32_e32 v65, v65, v241
	s_add_i32 s82, s17, 0xffffc000
	v_mfma_f32_32x32x16_bf16 v[32:47], a[240:243], a[176:179], v[32:47]
	ds_read_b64_tr_b16 v[82:83], v208 offset:0x2e00
	ds_read_b64_tr_b16 v[76:77], v208 offset:0x3000
	v_cvt_pk_bf16_f32 v87, v242, v243
	v_add_f32_e32 v64, v64, v242
	v_add_f32_e32 v65, v65, v243
	s_mov_b32 s83, s55
	v_mfma_f32_32x32x16_bf16 v[112:127], a[212:215], a[148:151], v[112:127]
	ds_read_b64_tr_b16 v[78:79], v208 offset:0x3800
	v_add_f32_e32 v64, v64, v198
	v_add_f32_e32 v65, v65, v199
	s_add_i32 s84, s17, 0xffffe000
	v_mfma_f32_32x32x16_bf16 v[96:111], a[212:215], a[180:183], v[96:111]
	ds_read_b64_tr_b16 v[72:73], v208 offset:0x3200
	v_add_f32_e32 v64, v64, v230
	v_add_f32_e32 v65, v65, v231
	s_mov_b32 s85, s57
	v_mfma_f32_32x32x16_bf16 v[48:63], a[244:247], a[148:151], v[48:63]
	ds_read_b64_tr_b16 v[74:75], v208 offset:0x3a00
	v_add_f32_e32 v64, v64, v232
	v_add_f32_e32 v65, v65, v233
	s_mov_b32 s86, s17
	v_mfma_f32_32x32x16_bf16 v[32:47], a[244:247], a[180:183], v[32:47]
	ds_read_b64_tr_b16 v[68:69], v208 offset:0x3400
	ds_read_b64_tr_b16 v[70:71], v208 offset:0x3c00
	v_add_f32_e32 v156, v64, v234
	v_add_f32_e32 v157, v65, v235
	s_mov_b32 s87, s31
	v_mfma_f32_32x32x16_bf16 v[112:127], a[216:219], a[152:155], v[112:127]
	ds_read_b64_tr_b16 v[64:65], v208 offset:0x3600
	v_cvt_pk_bf16_f32 v140, v141, v142
	v_add_f32_e32 v158, v238, v141
	v_add_f32_e32 v142, v239, v142
	v_mfma_f32_32x32x16_bf16 v[96:111], a[216:219], a[184:187], v[96:111]
	ds_read_b64_tr_b16 v[66:67], v208 offset:0x3e00
	v_cvt_pk_bf16_f32 v141, v143, v244
	v_add_f32_e32 v143, v158, v143
	v_add_f32_e32 v158, v142, v244
	v_mfma_f32_32x32x16_bf16 v[48:63], a[248:251], a[152:155], v[48:63]
	s_mov_b32 s88, s59
	v_cvt_pk_bf16_f32 v142, v245, v246
	v_add_f32_e32 v159, v143, v245
	v_add_f32_e32 v158, v158, v246
	v_mfma_f32_32x32x16_bf16 v[32:47], a[248:251], a[184:187], v[32:47]
	s_add_i32 s89, s17, 0xfffda080
	v_cvt_pk_bf16_f32 v143, v247, v248
	v_add_f32_e32 v159, v159, v247
	v_add_f32_e32 v158, v158, v248
	v_mfma_f32_32x32x16_bf16 v[112:127], a[220:223], a[156:159], v[112:127]
	s_mov_b32 s90, s61
	v_add_f32_e32 v159, v159, v148
	v_add_f32_e32 v158, v158, v149
	v_mfma_f32_32x32x16_bf16 v[96:111], a[220:223], a[188:191], v[96:111]
	v_add_f32_e32 v159, v159, v150
	v_add_f32_e32 v158, v158, v151
	v_mfma_f32_32x32x16_bf16 v[48:63], a[252:255], a[156:159], v[48:63]
	s_mov_b32 s91, s62
	v_add_f32_e32 v159, v159, v152
	v_add_f32_e32 v158, v158, v153
	v_mfma_f32_32x32x16_bf16 v[32:47], a[252:255], a[188:191], v[32:47]
	s_add_i32 s92, s17, 0xfffde080
	v_add_f32_e32 v159, v159, v154
	v_add_f32_e32 v158, v158, v155
	v_add_f32_e32 v156, v156, v157
	s_waitcnt vmcnt(0) lgkmcnt(0)
	s_barrier
	v_add_f32_e32 v158, v159, v158
	v_mov_b32_e32 v157, v156
	v_mov_b32_e32 v159, v158
	s_nop 0
	v_permlane32_swap_b32_e32 v156, v157
	v_permlane32_swap_b32_e32 v158, v159
	v_add_f32_e32 v156, v156, v157
	v_add_f32_e32 v158, v158, v159
	v_add_f32_e32 v197, v197, v156
	v_add_f32_e32 v196, v196, v158
	s_mov_b32 m0, s0
	v_mfma_f32_32x32x16_bf16 a[0:15], v[180:183], v[164:167], a[0:15]
	buffer_load_dwordx4 v209, s[4:7], s1 offen lds
	s_mov_b32 m0, s81
	v_mfma_f32_32x32x16_bf16 a[16:31], v[180:183], v[192:195], a[16:31]
	buffer_load_dwordx4 v210, s[4:7], s82 offen lds
	ds_read_b128 a[192:195], v204 offset:0
	s_mov_b32 m0, s83
	v_mfma_f32_32x32x16_bf16 a[32:47], v[184:187], v[164:167], a[32:47]
	buffer_load_dwordx4 v209, s[4:7], s84 offen lds
	ds_read_b128 a[196:199], v205 offset:0
	s_mov_b32 m0, s85
	v_mfma_f32_32x32x16_bf16 a[48:63], v[184:187], v[192:195], a[48:63]
	buffer_load_dwordx4 v210, s[4:7], s86 offen lds
	ds_read_b128 a[200:203], v206 offset:0
	s_mov_b32 m0, s87
	v_mfma_f32_32x32x16_bf16 a[64:79], v[176:179], v[164:167], a[64:79]
	buffer_load_dwordx4 v211, s[20:23], s19 offen lds
	ds_read_b128 a[204:207], v207 offset:0
	s_mov_b32 m0, s88
	v_mfma_f32_32x32x16_bf16 a[80:95], v[176:179], v[192:195], a[80:95]
	buffer_load_dwordx4 v211, s[20:23], s89 offen lds
	ds_read_b128 a[208:211], v204 offset:128
	s_mov_b32 m0, s90
	v_mfma_f32_32x32x16_bf16 a[96:111], v[188:191], v[164:167], a[96:111]
	buffer_load_dwordx4 v211, s[20:23], s24 offen lds
	ds_read_b128 a[212:215], v205 offset:128
	s_mov_b32 m0, s91
	v_mfma_f32_32x32x16_bf16 a[112:127], v[188:191], v[192:195], a[112:127]
	buffer_load_dwordx4 v211, s[20:23], s92 offen lds
	ds_read_b128 a[216:219], v206 offset:128
	v_mfma_f32_32x32x16_bf16 a[0:15], v[172:175], v[128:131], a[0:15]
	ds_read_b128 a[220:223], v207 offset:128
	v_max3_f32 v156, v112, v113, v48
	v_max3_f32 v157, v114, v115, v49
	v_max3_f32 v156, v156, v50, v51
	v_mfma_f32_32x32x16_bf16 a[16:31], v[172:175], v[144:147], a[16:31]
	ds_read_b128 a[224:227], v204 offset:8192
	v_max3_f32 v156, v156, v116, v117
	v_max3_f32 v157, v157, v118, v119
	v_max3_f32 v156, v156, v52, v53
	v_max3_f32 v157, v157, v54, v55
	v_mfma_f32_32x32x16_bf16 a[32:47], v[168:171], v[128:131], a[32:47]
	ds_read_b128 a[228:231], v205 offset:8192
	v_max3_f32 v156, v156, v120, v121
	v_max3_f32 v157, v157, v122, v123
	v_max3_f32 v156, v156, v56, v57
	v_max3_f32 v157, v157, v58, v59
	v_mfma_f32_32x32x16_bf16 a[48:63], v[168:171], v[144:147], a[48:63]
	ds_read_b128 a[232:235], v206 offset:8192
	v_max3_f32 v156, v156, v124, v125
	v_max3_f32 v157, v157, v126, v127
	v_max3_f32 v156, v156, v60, v61
	v_max3_f32 v157, v157, v62, v63
	v_mfma_f32_32x32x16_bf16 a[64:79], v[160:163], v[128:131], a[64:79]
	ds_read_b128 a[236:239], v207 offset:8192
	v_max3_f32 v158, v96, v97, v32
	v_max3_f32 v159, v98, v99, v33
	v_max3_f32 v158, v158, v34, v35
	v_mfma_f32_32x32x16_bf16 a[80:95], v[160:163], v[144:147], a[80:95]
	ds_read_b128 a[240:243], v204 offset:8320
	v_max3_f32 v158, v158, v100, v101
	v_max3_f32 v159, v159, v102, v103
	v_max3_f32 v158, v158, v36, v37
	v_max3_f32 v159, v159, v38, v39
	v_mfma_f32_32x32x16_bf16 a[96:111], v[136:139], v[128:131], a[96:111]
	ds_read_b128 a[244:247], v205 offset:8320
	v_max3_f32 v128, v158, v104, v105
	v_max3_f32 v129, v159, v106, v107
	v_max3_f32 v128, v128, v40, v41
	v_max3_f32 v129, v129, v42, v43
	v_mfma_f32_32x32x16_bf16 a[112:127], v[136:139], v[144:147], a[112:127]
	ds_read_b128 a[248:251], v206 offset:8320
	v_max3_f32 v128, v128, v108, v109
	v_max3_f32 v129, v129, v110, v111
	v_max3_f32 v128, v128, v44, v45
	v_max3_f32 v130, v129, v46, v47
	v_mfma_f32_32x32x16_bf16 a[0:15], v[132:135], v[84:87], a[0:15]
	ds_read_b128 a[252:255], v207 offset:8320
	v_max_f32_e32 v129, v156, v157
	v_mov_b32_e32 v131, v129
	s_nop 1
	v_permlane32_swap_b32_e32 v129, v131
	v_max_f32_e32 v129, v129, v131
	v_mfma_f32_32x32x16_bf16 a[16:31], v[132:135], v[140:143], a[16:31]
	v_max_f32_e32 v128, v128, v130
	v_mov_b32_e32 v130, v128
	s_nop 1
	v_permlane32_swap_b32_e32 v128, v130
	v_max_f32_e32 v128, v128, v130
	v_max_f32_e32 v130, v129, v129
	v_max_f32_e32 v131, v128, v128
	v_max_f32_e32 v130, v130, v131
	v_mfma_f32_32x32x16_bf16 a[32:47], v[92:95], v[84:87], a[32:47]
	v_cmp_lt_f32_e32 vcc, s79, v130
	s_cmp_lg_u64 vcc, 0
	s_cselect_b64 s[0:1], -1, 0
	s_cbranch_vccnz .LBB2_20
